# P8 routing tail: one returning atomic under the union of the four disjoint top-k lane masks instead of four serialized atomics; plus P7b epilogue ring and GA=168
# speedup vs baseline: 1.0005x; 1.0005x over previous
; __global__ void __launch_bounds__(NWAVES * 64, 2) fwd_kernel(Args a_unused) {
;     ...
;               for (int j = 0; j < 4; ++j) { float bv = val; int bi = e;
; #pragma unroll
;                   for (int off = 16; off >= 1; off >>= 1) { const float ov = __shfl_xor(bv, off); const int oi = __shfl_xor(bi, off); if (ov > bv || (ov == bv && oi < bi)) { bv = ov; bi = oi; } }
;                   tv[j] = bv; ti[j] = bi; if (e == bi) val = -INFINITY; }
;               const float e1 = __expf(tv[1] - tv[0]), e2 = __expf(tv[2] - tv[0]), e3 = __expf(tv[3] - tv[0]), inv = 1.0f / (1.0f + e1 + e2 + e3);
;               const float gt[4] = {inv, e1 * inv, e2 * inv, e3 * inv};
; #pragma unroll
;               for (int j = 0; j < 4; ++j) if (e == ti[j]) { const int ai = (row0 + row) * 4 + j; const unsigned rk = atomicAdd(ctl + CW_CNT + 16 * e, 1u);
;                   rt_e[ai] = e; rt_g[ai] = gt[j]; rt_r[ai] = (int)rk; } }
.LBB0_1951:
	s_or_b64 exec, exec, s[12:13]
	v_sub_f32_e32 v131, v131, v130
	v_mul_f32_e32 v131, 0x3fb8aa3b, v131
	v_exp_f32_e32 v194, v131
	v_sub_f32_e32 v131, v132, v130
	v_mul_f32_e32 v131, 0x3fb8aa3b, v131
	v_sub_f32_e32 v130, v193, v130
	v_exp_f32_e32 v132, v131
	v_mul_f32_e32 v130, 0x3fb8aa3b, v130
	v_exp_f32_e32 v130, v130
	v_add_f32_e32 v131, 1.0, v194
	v_add_f32_e32 v131, v131, v132
	v_add_f32_e32 v131, v131, v130
	v_div_scale_f32 v193, s[12:13], v131, v131, 1.0
	s_waitcnt lgkmcnt(0)
	v_rcp_f32_e32 v195, v193
	s_nop 0
	v_fma_f32 v196, -v193, v195, 1.0
	v_fmac_f32_e32 v195, v196, v195
	v_div_scale_f32 v196, vcc, 1.0, v131, 1.0
	v_mul_f32_e32 v197, v196, v195
	v_fma_f32 v198, -v193, v197, v196
	v_fmac_f32_e32 v197, v198, v195
	v_fma_f32 v193, -v193, v197, v196
	v_div_fmas_f32 v193, v193, v195, v197
	v_div_fixup_f32 v131, v193, v131, 1.0
	v_mul_f32_e32 v198, v194, v131
	v_mul_f32_e32 v132, v132, v131
	v_mul_f32_e32 v195, v130, v131
	v_cmp_eq_u32_e64 s[12:13], v235, v133
	v_add_u32_e32 v196, -1, v192
	v_add_u32_e32 v197, -2, v192
	v_add_u32_e32 v199, -3, v192
	v_cndmask_b32_e64 v195, v195, v132, s[10:11]
	v_cndmask_b32_e64 v130, v192, v196, s[10:11]
	v_cndmask_b32_e64 v195, v195, v198, s[8:9]
	v_cndmask_b32_e64 v130, v130, v197, s[8:9]
	v_cndmask_b32_e64 v195, v195, v131, s[6:7]
	v_cndmask_b32_e64 v130, v130, v199, s[6:7]
	s_or_b64 s[8:9], s[6:7], s[8:9]
	s_or_b64 s[10:11], s[10:11], s[12:13]
	s_or_b64 s[8:9], s[8:9], s[10:11]
	s_and_saveexec_b64 s[6:7], s[8:9]
	s_cbranch_execz .LBB0_1862
	global_atomic_add v193, v[142:143], v240, off sc0
	v_ashrrev_i32_e32 v131, 31, v130
	v_lshlrev_b64 v[130:131], 2, v[130:131]
	v_lshl_add_u64 v[132:133], s[20:21], 0, v[130:131]
	v_lshl_add_u64 v[196:197], s[22:23], 0, v[130:131]
	v_lshl_add_u64 v[198:199], s[24:25], 0, v[130:131]
	global_store_dword v[132:133], v235, off
	global_store_dword v[196:197], v195, off
	s_waitcnt vmcnt(2)
	global_store_dword v[198:199], v193, off
	s_branch .LBB0_1862
